# grid barrier: the agent-scope acquire invalidate (buffer_inv sc1) issued once before the arrival atomic instead of after the release (workgroup issues no cacheable loads while waiting), removing it fr
# speedup vs baseline: 1.0082x; 1.0045x over previous
.LBB0_224:
	v_readlane_b32 s0, v254, 37
	s_lshl_b32 s0, s0, 8
	v_readlane_b32 s4, v254, 34
	v_readlane_b32 s5, v254, 35
	s_add_u32 s0, s4, s0
	s_addc_u32 s1, s5, 0
	buffer_inv sc1
	v_mov_b32_e32 v2, 0x1000
	v_mov_b32_e32 v4, 1
	global_atomic_add v4, v2, v4, s[0:1] offset:1024 sc0
	v_cvt_f32_u32_e32 v2, v3
	v_sub_u32_e32 v5, 0, v3
	v_rcp_iflag_f32_e32 v2, v2
	s_nop 0
	v_mul_f32_e32 v2, 0x4f7ffffe, v2
	v_cvt_u32_f32_e32 v2, v2
	v_mul_lo_u32 v5, v5, v2
	v_mul_hi_u32 v5, v2, v5
	v_add_u32_e32 v2, v2, v5
	s_waitcnt vmcnt(0)
	v_mul_hi_u32 v2, v4, v2
	v_mul_lo_u32 v5, v2, v3
	v_sub_u32_e32 v5, v4, v5
	v_add_u32_e32 v6, 1, v2
	v_cmp_ge_u32_e32 vcc, v5, v3
	v_add_u32_e32 v4, 1, v4
	s_nop 0
	v_cndmask_b32_e32 v2, v2, v6, vcc
	v_sub_u32_e32 v6, v5, v3
	v_cndmask_b32_e32 v5, v5, v6, vcc
	v_add_u32_e32 v6, 1, v2
	v_cmp_ge_u32_e32 vcc, v5, v3
	s_nop 1
	v_cndmask_b32_e32 v2, v2, v6, vcc
	v_mul_lo_u32 v5, v3, v2
	v_add_u32_e32 v3, v5, v3
	v_cmp_ne_u32_e32 vcc, v4, v3
	s_and_saveexec_b64 s[4:5], vcc
	s_xor_b64 s[4:5], exec, s[4:5]
	s_cbranch_execz .LBB0_238
	s_waitcnt lgkmcnt(0)
	v_mov_b32_e32 v1, 0x2000
	global_load_dword v1, v1, s[0:1] offset:1024 sc1
	s_add_u32 s14, s0, 0x2400
	s_addc_u32 s15, s1, 0
	s_waitcnt vmcnt(0)
	v_cmp_eq_u32_e32 vcc, v1, v2
	s_and_saveexec_b64 s[6:7], vcc
	s_cbranch_execz .LBB0_237
	s_add_u32 s10, s94, 0x4200
	s_addc_u32 s11, s95, 0
	s_mov_b32 s12, 1
	s_mov_b64 s[16:17], 0
	v_mov_b32_e32 v1, 0
	s_branch .LBB0_228

.LBB0_237:
	s_or_b64 exec, exec, s[6:7]
	s_waitcnt vmcnt(0)
	s_waitcnt vmcnt(0)

.LBB0_255:
	s_or_b64 exec, exec, s[4:5]
	v_mov_b32_e32 v1, 0x2000
	v_mov_b32_e32 v2, 1
	s_waitcnt vmcnt(0)
	global_atomic_add v1, v2, s[0:1] offset:1024
	s_waitcnt vmcnt(0)

.LBB0_280:
	v_readlane_b32 s2, v254, 37
	s_lshl_b32 s2, s2, 8
	v_readlane_b32 s4, v254, 34
	v_readlane_b32 s5, v254, 35
	s_add_u32 s2, s4, s2
	s_addc_u32 s3, s5, 0
	buffer_inv sc1
	v_mov_b32_e32 v2, 0x1000
	v_mov_b32_e32 v4, 1
	global_atomic_add v4, v2, v4, s[2:3] offset:1024 sc0
	v_cvt_f32_u32_e32 v2, v3
	v_sub_u32_e32 v5, 0, v3
	v_rcp_iflag_f32_e32 v2, v2
	s_nop 0
	v_mul_f32_e32 v2, 0x4f7ffffe, v2
	v_cvt_u32_f32_e32 v2, v2
	v_mul_lo_u32 v5, v5, v2
	v_mul_hi_u32 v5, v2, v5
	v_add_u32_e32 v2, v2, v5
	s_waitcnt vmcnt(0)
	v_mul_hi_u32 v2, v4, v2
	v_mul_lo_u32 v5, v2, v3
	v_sub_u32_e32 v5, v4, v5
	v_add_u32_e32 v6, 1, v2
	v_cmp_ge_u32_e32 vcc, v5, v3
	v_add_u32_e32 v4, 1, v4
	s_nop 0
	v_cndmask_b32_e32 v2, v2, v6, vcc
	v_sub_u32_e32 v6, v5, v3
	v_cndmask_b32_e32 v5, v5, v6, vcc
	v_add_u32_e32 v6, 1, v2
	v_cmp_ge_u32_e32 vcc, v5, v3
	s_nop 1
	v_cndmask_b32_e32 v2, v2, v6, vcc
	v_mul_lo_u32 v5, v3, v2
	v_add_u32_e32 v3, v5, v3
	v_cmp_ne_u32_e32 vcc, v4, v3
	s_and_saveexec_b64 s[4:5], vcc
	s_xor_b64 s[4:5], exec, s[4:5]
	s_cbranch_execz .LBB0_294
	s_waitcnt lgkmcnt(0)
	v_mov_b32_e32 v1, 0x2000
	global_load_dword v1, v1, s[2:3] offset:1024 sc1
	s_add_u32 s14, s2, 0x2400
	s_addc_u32 s15, s3, 0
	s_waitcnt vmcnt(0)
	v_cmp_eq_u32_e32 vcc, v1, v2
	s_and_saveexec_b64 s[6:7], vcc
	s_cbranch_execz .LBB0_293
	s_add_u32 s10, s94, 0x4200
	s_addc_u32 s11, s95, 0
	s_mov_b32 s12, 1
	s_mov_b64 s[16:17], 0
	v_mov_b32_e32 v1, 0
	s_branch .LBB0_284

.LBB0_311:
	s_or_b64 exec, exec, s[4:5]
	v_mov_b32_e32 v1, 0x2000
	v_mov_b32_e32 v2, 1
	s_waitcnt vmcnt(0)
	global_atomic_add v1, v2, s[2:3] offset:1024
	s_waitcnt vmcnt(0)

.LBB0_430:
	v_readlane_b32 s2, v254, 37
	s_lshl_b32 s2, s2, 8
	v_readlane_b32 s4, v254, 34
	v_readlane_b32 s5, v254, 35
	s_add_u32 s2, s4, s2
	s_addc_u32 s3, s5, 0
	buffer_inv sc1
	v_mov_b32_e32 v2, 0x1000
	v_mov_b32_e32 v4, 1
	global_atomic_add v4, v2, v4, s[2:3] offset:1024 sc0
	v_cvt_f32_u32_e32 v2, v3
	v_sub_u32_e32 v5, 0, v3
	v_rcp_iflag_f32_e32 v2, v2
	s_nop 0
	v_mul_f32_e32 v2, 0x4f7ffffe, v2
	v_cvt_u32_f32_e32 v2, v2
	v_mul_lo_u32 v5, v5, v2
	v_mul_hi_u32 v5, v2, v5
	v_add_u32_e32 v2, v2, v5
	s_waitcnt vmcnt(0)
	v_mul_hi_u32 v2, v4, v2
	v_mul_lo_u32 v5, v2, v3
	v_sub_u32_e32 v5, v4, v5
	v_add_u32_e32 v6, 1, v2
	v_cmp_ge_u32_e32 vcc, v5, v3
	v_add_u32_e32 v4, 1, v4
	s_nop 0
	v_cndmask_b32_e32 v2, v2, v6, vcc
	v_sub_u32_e32 v6, v5, v3
	v_cndmask_b32_e32 v5, v5, v6, vcc
	v_add_u32_e32 v6, 1, v2
	v_cmp_ge_u32_e32 vcc, v5, v3
	s_nop 1
	v_cndmask_b32_e32 v2, v2, v6, vcc
	v_mul_lo_u32 v5, v3, v2
	v_add_u32_e32 v3, v5, v3
	v_cmp_ne_u32_e32 vcc, v4, v3
	s_and_saveexec_b64 s[4:5], vcc
	s_xor_b64 s[4:5], exec, s[4:5]
	s_cbranch_execz .LBB0_444
	s_waitcnt lgkmcnt(0)
	v_mov_b32_e32 v1, 0x2000
	global_load_dword v1, v1, s[2:3] offset:1024 sc1
	s_add_u32 s30, s2, 0x2400
	s_addc_u32 s31, s3, 0
	s_waitcnt vmcnt(0)
	v_cmp_eq_u32_e32 vcc, v1, v2
	s_and_saveexec_b64 s[6:7], vcc
	s_cbranch_execz .LBB0_443
	s_add_u32 s14, s94, 0x4200
	s_addc_u32 s15, s95, 0
	s_mov_b32 s10, 1
	s_mov_b64 s[34:35], 0
	v_mov_b32_e32 v1, 0
	s_branch .LBB0_434

.LBB0_1243:
	v_readlane_b32 s0, v254, 37
	s_lshl_b32 s0, s0, 8
	v_readlane_b32 s4, v254, 34
	v_readlane_b32 s5, v254, 35
	s_add_u32 s0, s4, s0
	s_addc_u32 s1, s5, 0
	buffer_inv sc1
	v_mov_b32_e32 v2, 0x1000
	v_mov_b32_e32 v4, 1
	global_atomic_add v4, v2, v4, s[0:1] offset:1024 sc0
	v_cvt_f32_u32_e32 v2, v3
	v_sub_u32_e32 v5, 0, v3
	v_rcp_iflag_f32_e32 v2, v2
	s_nop 0
	v_mul_f32_e32 v2, 0x4f7ffffe, v2
	v_cvt_u32_f32_e32 v2, v2
	v_mul_lo_u32 v5, v5, v2
	v_mul_hi_u32 v5, v2, v5
	v_add_u32_e32 v2, v2, v5
	s_waitcnt vmcnt(0)
	v_mul_hi_u32 v2, v4, v2
	v_mul_lo_u32 v5, v2, v3
	v_sub_u32_e32 v5, v4, v5
	v_add_u32_e32 v6, 1, v2
	v_cmp_ge_u32_e32 vcc, v5, v3
	v_add_u32_e32 v4, 1, v4
	s_nop 0
	v_cndmask_b32_e32 v2, v2, v6, vcc
	v_sub_u32_e32 v6, v5, v3
	v_cndmask_b32_e32 v5, v5, v6, vcc
	v_add_u32_e32 v6, 1, v2
	v_cmp_ge_u32_e32 vcc, v5, v3
	s_nop 1
	v_cndmask_b32_e32 v2, v2, v6, vcc
	v_mul_lo_u32 v5, v3, v2
	v_add_u32_e32 v3, v5, v3
	v_cmp_ne_u32_e32 vcc, v4, v3
	s_and_saveexec_b64 s[4:5], vcc
	s_xor_b64 s[4:5], exec, s[4:5]
	s_cbranch_execz .LBB0_1257
	s_waitcnt lgkmcnt(0)
	v_mov_b32_e32 v1, 0x2000
	global_load_dword v1, v1, s[0:1] offset:1024 sc1
	s_add_u32 s34, s0, 0x2400
	s_addc_u32 s35, s1, 0
	s_waitcnt vmcnt(0)
	v_cmp_eq_u32_e32 vcc, v1, v2
	s_and_saveexec_b64 s[6:7], vcc
	s_cbranch_execz .LBB0_1256
	s_add_u32 s30, s94, 0x4200
	s_addc_u32 s31, s95, 0
	s_mov_b32 s10, 1
	s_mov_b64 s[56:57], 0
	v_mov_b32_e32 v1, 0
	s_branch .LBB0_1247

.LBB0_1322:
	v_readlane_b32 s2, v254, 37
	s_lshl_b32 s2, s2, 8
	v_readlane_b32 s4, v254, 34
	v_readlane_b32 s5, v254, 35
	s_add_u32 s2, s4, s2
	s_addc_u32 s3, s5, 0
	buffer_inv sc1
	v_mov_b32_e32 v2, 0x1000
	v_mov_b32_e32 v4, 1
	global_atomic_add v4, v2, v4, s[2:3] offset:1024 sc0
	v_cvt_f32_u32_e32 v2, v3
	v_sub_u32_e32 v5, 0, v3
	v_rcp_iflag_f32_e32 v2, v2
	s_nop 0
	v_mul_f32_e32 v2, 0x4f7ffffe, v2
	v_cvt_u32_f32_e32 v2, v2
	v_mul_lo_u32 v5, v5, v2
	v_mul_hi_u32 v5, v2, v5
	v_add_u32_e32 v2, v2, v5
	s_waitcnt vmcnt(0)
	v_mul_hi_u32 v2, v4, v2
	v_mul_lo_u32 v5, v2, v3
	v_sub_u32_e32 v5, v4, v5
	v_add_u32_e32 v6, 1, v2
	v_cmp_ge_u32_e32 vcc, v5, v3
	v_add_u32_e32 v4, 1, v4
	s_nop 0
	v_cndmask_b32_e32 v2, v2, v6, vcc
	v_sub_u32_e32 v6, v5, v3
	v_cndmask_b32_e32 v5, v5, v6, vcc
	v_add_u32_e32 v6, 1, v2
	v_cmp_ge_u32_e32 vcc, v5, v3
	s_nop 1
	v_cndmask_b32_e32 v2, v2, v6, vcc
	v_mul_lo_u32 v5, v3, v2
	v_add_u32_e32 v3, v5, v3
	v_cmp_ne_u32_e32 vcc, v4, v3
	s_and_saveexec_b64 s[4:5], vcc
	s_xor_b64 s[4:5], exec, s[4:5]
	s_cbranch_execz .LBB0_1336
	s_waitcnt lgkmcnt(0)
	v_mov_b32_e32 v1, 0x2000
	global_load_dword v1, v1, s[2:3] offset:1024 sc1
	s_add_u32 s34, s2, 0x2400
	s_addc_u32 s35, s3, 0
	s_waitcnt vmcnt(0)
	v_cmp_eq_u32_e32 vcc, v1, v2
	s_and_saveexec_b64 s[6:7], vcc
	s_cbranch_execz .LBB0_1335
	s_add_u32 s30, s94, 0x4200
	s_addc_u32 s31, s95, 0
	s_mov_b32 s10, 1
	s_mov_b64 s[56:57], 0
	v_mov_b32_e32 v1, 0
	s_branch .LBB0_1326

.LBB0_1397:
	v_readlane_b32 s2, v254, 37
	s_lshl_b32 s2, s2, 8
	v_readlane_b32 s4, v254, 34
	v_readlane_b32 s5, v254, 35
	s_add_u32 s2, s4, s2
	s_addc_u32 s3, s5, 0
	buffer_inv sc1
	v_mov_b32_e32 v2, 0x1000
	v_mov_b32_e32 v4, 1
	global_atomic_add v4, v2, v4, s[2:3] offset:1024 sc0
	v_cvt_f32_u32_e32 v2, v3
	v_sub_u32_e32 v5, 0, v3
	v_rcp_iflag_f32_e32 v2, v2
	s_nop 0
	v_mul_f32_e32 v2, 0x4f7ffffe, v2
	v_cvt_u32_f32_e32 v2, v2
	v_mul_lo_u32 v5, v5, v2
	v_mul_hi_u32 v5, v2, v5
	v_add_u32_e32 v2, v2, v5
	s_waitcnt vmcnt(0)
	v_mul_hi_u32 v2, v4, v2
	v_mul_lo_u32 v5, v2, v3
	v_sub_u32_e32 v5, v4, v5
	v_add_u32_e32 v6, 1, v2
	v_cmp_ge_u32_e32 vcc, v5, v3
	v_add_u32_e32 v4, 1, v4
	s_nop 0
	v_cndmask_b32_e32 v2, v2, v6, vcc
	v_sub_u32_e32 v6, v5, v3
	v_cndmask_b32_e32 v5, v5, v6, vcc
	v_add_u32_e32 v6, 1, v2
	v_cmp_ge_u32_e32 vcc, v5, v3
	s_nop 1
	v_cndmask_b32_e32 v2, v2, v6, vcc
	v_mul_lo_u32 v5, v3, v2
	v_add_u32_e32 v3, v5, v3
	v_cmp_ne_u32_e32 vcc, v4, v3
	s_and_saveexec_b64 s[4:5], vcc
	s_xor_b64 s[4:5], exec, s[4:5]
	s_cbranch_execz .LBB0_1411
	s_waitcnt lgkmcnt(0)
	v_mov_b32_e32 v1, 0x2000
	global_load_dword v1, v1, s[2:3] offset:1024 sc1
	s_add_u32 s30, s2, 0x2400
	s_addc_u32 s31, s3, 0
	s_waitcnt vmcnt(0)
	v_cmp_eq_u32_e32 vcc, v1, v2
	s_and_saveexec_b64 s[6:7], vcc
	s_cbranch_execz .LBB0_1410
	s_add_u32 s12, s94, 0x4200
	s_addc_u32 s13, s95, 0
	s_mov_b32 s10, 1
	s_mov_b64 s[34:35], 0
	v_mov_b32_e32 v1, 0
	s_branch .LBB0_1401

.LBB0_1792:
	v_readlane_b32 s2, v254, 37
	s_lshl_b32 s2, s2, 8
	v_readlane_b32 s4, v254, 34
	v_readlane_b32 s5, v254, 35
	s_add_u32 s2, s4, s2
	s_addc_u32 s3, s5, 0
	buffer_inv sc1
	v_mov_b32_e32 v2, 0x1000
	v_mov_b32_e32 v4, 1
	global_atomic_add v4, v2, v4, s[2:3] offset:1024 sc0
	v_cvt_f32_u32_e32 v2, v3
	v_sub_u32_e32 v5, 0, v3
	v_rcp_iflag_f32_e32 v2, v2
	s_nop 0
	v_mul_f32_e32 v2, 0x4f7ffffe, v2
	v_cvt_u32_f32_e32 v2, v2
	v_mul_lo_u32 v5, v5, v2
	v_mul_hi_u32 v5, v2, v5
	v_add_u32_e32 v2, v2, v5
	s_waitcnt vmcnt(0)
	v_mul_hi_u32 v2, v4, v2
	v_mul_lo_u32 v5, v2, v3
	v_sub_u32_e32 v5, v4, v5
	v_add_u32_e32 v6, 1, v2
	v_cmp_ge_u32_e32 vcc, v5, v3
	v_add_u32_e32 v4, 1, v4
	s_nop 0
	v_cndmask_b32_e32 v2, v2, v6, vcc
	v_sub_u32_e32 v6, v5, v3
	v_cndmask_b32_e32 v5, v5, v6, vcc
	v_add_u32_e32 v6, 1, v2
	v_cmp_ge_u32_e32 vcc, v5, v3
	s_nop 1
	v_cndmask_b32_e32 v2, v2, v6, vcc
	v_mul_lo_u32 v5, v3, v2
	v_add_u32_e32 v3, v5, v3
	v_cmp_ne_u32_e32 vcc, v4, v3
	s_and_saveexec_b64 s[4:5], vcc
	s_xor_b64 s[4:5], exec, s[4:5]
	s_cbranch_execz .LBB0_1806
	s_waitcnt lgkmcnt(0)
	v_mov_b32_e32 v1, 0x2000
	global_load_dword v1, v1, s[2:3] offset:1024 sc1
	s_add_u32 s34, s2, 0x2400
	s_addc_u32 s35, s3, 0
	s_waitcnt vmcnt(0)
	v_cmp_eq_u32_e32 vcc, v1, v2
	s_and_saveexec_b64 s[6:7], vcc
	s_cbranch_execz .LBB0_1805
	s_add_u32 s30, s94, 0x4200
	s_addc_u32 s31, s95, 0
	s_mov_b32 s10, 1
	s_mov_b64 s[68:69], 0
	v_mov_b32_e32 v1, 0
	s_branch .LBB0_1796

.LBB0_1848:
	v_readlane_b32 s2, v254, 37
	s_lshl_b32 s2, s2, 8
	v_readlane_b32 s4, v254, 34
	v_readlane_b32 s5, v254, 35
	s_add_u32 s2, s4, s2
	s_addc_u32 s3, s5, 0
	buffer_inv sc1
	v_mov_b32_e32 v2, 0x1000
	v_mov_b32_e32 v4, 1
	global_atomic_add v4, v2, v4, s[2:3] offset:1024 sc0
	v_cvt_f32_u32_e32 v2, v3
	v_sub_u32_e32 v5, 0, v3
	v_rcp_iflag_f32_e32 v2, v2
	s_nop 0
	v_mul_f32_e32 v2, 0x4f7ffffe, v2
	v_cvt_u32_f32_e32 v2, v2
	v_mul_lo_u32 v5, v5, v2
	v_mul_hi_u32 v5, v2, v5
	v_add_u32_e32 v2, v2, v5
	s_waitcnt vmcnt(0)
	v_mul_hi_u32 v2, v4, v2
	v_mul_lo_u32 v5, v2, v3
	v_sub_u32_e32 v5, v4, v5
	v_add_u32_e32 v6, 1, v2
	v_cmp_ge_u32_e32 vcc, v5, v3
	v_add_u32_e32 v4, 1, v4
	s_nop 0
	v_cndmask_b32_e32 v2, v2, v6, vcc
	v_sub_u32_e32 v6, v5, v3
	v_cndmask_b32_e32 v5, v5, v6, vcc
	v_add_u32_e32 v6, 1, v2
	v_cmp_ge_u32_e32 vcc, v5, v3
	s_nop 1
	v_cndmask_b32_e32 v2, v2, v6, vcc
	v_mul_lo_u32 v5, v3, v2
	v_add_u32_e32 v3, v5, v3
	v_cmp_ne_u32_e32 vcc, v4, v3
	s_and_saveexec_b64 s[4:5], vcc
	s_xor_b64 s[4:5], exec, s[4:5]
	s_cbranch_execz .LBB0_1862
	s_waitcnt lgkmcnt(0)
	v_mov_b32_e32 v1, 0x2000
	global_load_dword v1, v1, s[2:3] offset:1024 sc1
	s_add_u32 s30, s2, 0x2400
	s_addc_u32 s31, s3, 0
	s_waitcnt vmcnt(0)
	v_cmp_eq_u32_e32 vcc, v1, v2
	s_and_saveexec_b64 s[6:7], vcc
	s_cbranch_execz .LBB0_1861
	s_add_u32 s20, s94, 0x4200
	s_addc_u32 s21, s95, 0
	s_mov_b32 s10, 1
	s_mov_b64 s[34:35], 0
	v_mov_b32_e32 v1, 0
	s_branch .LBB0_1852

.LBB0_1998:
	v_readlane_b32 s2, v254, 37
	s_lshl_b32 s2, s2, 8
	v_readlane_b32 s4, v254, 34
	v_readlane_b32 s5, v254, 35
	s_add_u32 s2, s4, s2
	s_addc_u32 s3, s5, 0
	buffer_inv sc1
	v_mov_b32_e32 v2, 0x1000
	v_mov_b32_e32 v4, 1
	global_atomic_add v4, v2, v4, s[2:3] offset:1024 sc0
	v_cvt_f32_u32_e32 v2, v3
	v_sub_u32_e32 v5, 0, v3
	v_rcp_iflag_f32_e32 v2, v2
	s_nop 0
	v_mul_f32_e32 v2, 0x4f7ffffe, v2
	v_cvt_u32_f32_e32 v2, v2
	v_mul_lo_u32 v5, v5, v2
	v_mul_hi_u32 v5, v2, v5
	v_add_u32_e32 v2, v2, v5
	s_waitcnt vmcnt(0)
	v_mul_hi_u32 v2, v4, v2
	v_mul_lo_u32 v5, v2, v3
	v_sub_u32_e32 v5, v4, v5
	v_add_u32_e32 v6, 1, v2
	v_cmp_ge_u32_e32 vcc, v5, v3
	v_add_u32_e32 v4, 1, v4
	s_nop 0
	v_cndmask_b32_e32 v2, v2, v6, vcc
	v_sub_u32_e32 v6, v5, v3
	v_cndmask_b32_e32 v5, v5, v6, vcc
	v_add_u32_e32 v6, 1, v2
	v_cmp_ge_u32_e32 vcc, v5, v3
	s_nop 1
	v_cndmask_b32_e32 v2, v2, v6, vcc
	v_mul_lo_u32 v5, v3, v2
	v_add_u32_e32 v3, v5, v3
	v_cmp_ne_u32_e32 vcc, v4, v3
	s_and_saveexec_b64 s[4:5], vcc
	s_xor_b64 s[4:5], exec, s[4:5]
	s_cbranch_execz .LBB0_2012
	s_waitcnt lgkmcnt(0)
	v_mov_b32_e32 v1, 0x2000
	global_load_dword v1, v1, s[2:3] offset:1024 sc1
	s_add_u32 s26, s2, 0x2400
	s_addc_u32 s27, s3, 0
	s_waitcnt vmcnt(0)
	v_cmp_eq_u32_e32 vcc, v1, v2
	s_and_saveexec_b64 s[6:7], vcc
	s_cbranch_execz .LBB0_2011
	s_add_u32 s20, s94, 0x4200
	s_addc_u32 s21, s95, 0
	s_mov_b32 s10, 1
	s_mov_b64 s[30:31], 0
	v_mov_b32_e32 v1, 0
	s_branch .LBB0_2002

.LBB0_2811:
	v_readlane_b32 s0, v254, 37
	s_lshl_b32 s0, s0, 8
	v_readlane_b32 s4, v254, 34
	v_readlane_b32 s5, v254, 35
	s_add_u32 s0, s4, s0
	s_addc_u32 s1, s5, 0
	buffer_inv sc1
	v_mov_b32_e32 v2, 0x1000
	v_mov_b32_e32 v4, 1
	global_atomic_add v4, v2, v4, s[0:1] offset:1024 sc0
	v_cvt_f32_u32_e32 v2, v3
	v_sub_u32_e32 v5, 0, v3
	v_rcp_iflag_f32_e32 v2, v2
	s_nop 0
	v_mul_f32_e32 v2, 0x4f7ffffe, v2
	v_cvt_u32_f32_e32 v2, v2
	v_mul_lo_u32 v5, v5, v2
	v_mul_hi_u32 v5, v2, v5
	v_add_u32_e32 v2, v2, v5
	s_waitcnt vmcnt(0)
	v_mul_hi_u32 v2, v4, v2
	v_mul_lo_u32 v5, v2, v3
	v_sub_u32_e32 v5, v4, v5
	v_add_u32_e32 v6, 1, v2
	v_cmp_ge_u32_e32 vcc, v5, v3
	v_add_u32_e32 v4, 1, v4
	s_nop 0
	v_cndmask_b32_e32 v2, v2, v6, vcc
	v_sub_u32_e32 v6, v5, v3
	v_cndmask_b32_e32 v5, v5, v6, vcc
	v_add_u32_e32 v6, 1, v2
	v_cmp_ge_u32_e32 vcc, v5, v3
	s_nop 1
	v_cndmask_b32_e32 v2, v2, v6, vcc
	v_mul_lo_u32 v5, v3, v2
	v_add_u32_e32 v3, v5, v3
	v_cmp_ne_u32_e32 vcc, v4, v3
	s_and_saveexec_b64 s[4:5], vcc
	s_xor_b64 s[4:5], exec, s[4:5]
	s_cbranch_execz .LBB0_2825
	s_waitcnt lgkmcnt(0)
	v_mov_b32_e32 v1, 0x2000
	global_load_dword v1, v1, s[0:1] offset:1024 sc1
	s_add_u32 s18, s0, 0x2400
	s_addc_u32 s19, s1, 0
	s_waitcnt vmcnt(0)
	v_cmp_eq_u32_e32 vcc, v1, v2
	s_and_saveexec_b64 s[6:7], vcc
	s_cbranch_execz .LBB0_2824
	s_add_u32 s16, s94, 0x4200
	s_addc_u32 s17, s95, 0
	s_mov_b32 s10, 1
	s_mov_b64 s[20:21], 0
	v_mov_b32_e32 v1, 0
	s_branch .LBB0_2815

.LBB0_2890:
	v_readlane_b32 s2, v254, 37
	s_lshl_b32 s2, s2, 8
	v_readlane_b32 s4, v254, 34
	v_readlane_b32 s5, v254, 35
	s_add_u32 s2, s4, s2
	s_addc_u32 s3, s5, 0
	buffer_inv sc1
	v_mov_b32_e32 v2, 0x1000
	v_mov_b32_e32 v4, 1
	global_atomic_add v4, v2, v4, s[2:3] offset:1024 sc0
	v_cvt_f32_u32_e32 v2, v3
	v_sub_u32_e32 v5, 0, v3
	v_rcp_iflag_f32_e32 v2, v2
	s_nop 0
	v_mul_f32_e32 v2, 0x4f7ffffe, v2
	v_cvt_u32_f32_e32 v2, v2
	v_mul_lo_u32 v5, v5, v2
	v_mul_hi_u32 v5, v2, v5
	v_add_u32_e32 v2, v2, v5
	s_waitcnt vmcnt(0)
	v_mul_hi_u32 v2, v4, v2
	v_mul_lo_u32 v5, v2, v3
	v_sub_u32_e32 v5, v4, v5
	v_add_u32_e32 v6, 1, v2
	v_cmp_ge_u32_e32 vcc, v5, v3
	v_add_u32_e32 v4, 1, v4
	s_nop 0
	v_cndmask_b32_e32 v2, v2, v6, vcc
	v_sub_u32_e32 v6, v5, v3
	v_cndmask_b32_e32 v5, v5, v6, vcc
	v_add_u32_e32 v6, 1, v2
	v_cmp_ge_u32_e32 vcc, v5, v3
	s_nop 1
	v_cndmask_b32_e32 v2, v2, v6, vcc
	v_mul_lo_u32 v5, v3, v2
	v_add_u32_e32 v3, v5, v3
	v_cmp_ne_u32_e32 vcc, v4, v3
	s_and_saveexec_b64 s[4:5], vcc
	s_xor_b64 s[4:5], exec, s[4:5]
	s_cbranch_execz .LBB0_2904
	s_waitcnt lgkmcnt(0)
	v_mov_b32_e32 v1, 0x2000
	global_load_dword v1, v1, s[2:3] offset:1024 sc1
	s_add_u32 s14, s2, 0x2400
	s_addc_u32 s15, s3, 0
	s_waitcnt vmcnt(0)
	v_cmp_eq_u32_e32 vcc, v1, v2
	s_and_saveexec_b64 s[6:7], vcc
	s_cbranch_execz .LBB0_2903
	s_add_u32 s10, s94, 0x4200
	s_addc_u32 s11, s95, 0
	s_mov_b32 s22, 1
	s_mov_b64 s[16:17], 0
	v_mov_b32_e32 v1, 0
	s_branch .LBB0_2894

.LBB0_2965:
	v_readlane_b32 s2, v254, 37
	s_lshl_b32 s2, s2, 8
	v_readlane_b32 s4, v254, 34
	v_readlane_b32 s5, v254, 35
	s_add_u32 s2, s4, s2
	s_addc_u32 s3, s5, 0
	buffer_inv sc1
	v_mov_b32_e32 v2, 0x1000
	v_mov_b32_e32 v4, 1
	global_atomic_add v4, v2, v4, s[2:3] offset:1024 sc0
	v_cvt_f32_u32_e32 v2, v3
	v_sub_u32_e32 v5, 0, v3
	v_rcp_iflag_f32_e32 v2, v2
	s_nop 0
	v_mul_f32_e32 v2, 0x4f7ffffe, v2
	v_cvt_u32_f32_e32 v2, v2
	v_mul_lo_u32 v5, v5, v2
	v_mul_hi_u32 v5, v2, v5
	v_add_u32_e32 v2, v2, v5
	s_waitcnt vmcnt(0)
	v_mul_hi_u32 v2, v4, v2
	v_mul_lo_u32 v5, v2, v3
	v_sub_u32_e32 v5, v4, v5
	v_add_u32_e32 v6, 1, v2
	v_cmp_ge_u32_e32 vcc, v5, v3
	v_add_u32_e32 v4, 1, v4
	s_nop 0
	v_cndmask_b32_e32 v2, v2, v6, vcc
	v_sub_u32_e32 v6, v5, v3
	v_cndmask_b32_e32 v5, v5, v6, vcc
	v_add_u32_e32 v6, 1, v2
	v_cmp_ge_u32_e32 vcc, v5, v3
	s_nop 1
	v_cndmask_b32_e32 v2, v2, v6, vcc
	v_mul_lo_u32 v5, v3, v2
	v_add_u32_e32 v3, v5, v3
	v_cmp_ne_u32_e32 vcc, v4, v3
	s_and_saveexec_b64 s[4:5], vcc
	s_xor_b64 s[4:5], exec, s[4:5]
	s_cbranch_execz .LBB0_2979
	s_waitcnt lgkmcnt(0)
	v_mov_b32_e32 v1, 0x2000
	global_load_dword v1, v1, s[2:3] offset:1024 sc1
	s_add_u32 s12, s2, 0x2400
	s_addc_u32 s13, s3, 0
	s_waitcnt vmcnt(0)
	v_cmp_eq_u32_e32 vcc, v1, v2
	s_and_saveexec_b64 s[6:7], vcc
	s_cbranch_execz .LBB0_2978
	s_add_u32 s10, s94, 0x4200
	s_addc_u32 s11, s95, 0
	s_mov_b32 s22, 1
	s_mov_b64 s[14:15], 0
	v_mov_b32_e32 v1, 0
	s_branch .LBB0_2969

.LBB0_3031:
	v_readlane_b32 s2, v254, 37
	s_lshl_b32 s2, s2, 8
	v_readlane_b32 s4, v254, 34
	v_readlane_b32 s5, v254, 35
	s_add_u32 s2, s4, s2
	s_addc_u32 s3, s5, 0
	buffer_inv sc1
	v_mov_b32_e32 v2, 0x1000
	v_mov_b32_e32 v4, 1
	global_atomic_add v4, v2, v4, s[2:3] offset:1024 sc0
	v_cvt_f32_u32_e32 v2, v3
	v_sub_u32_e32 v5, 0, v3
	v_rcp_iflag_f32_e32 v2, v2
	s_nop 0
	v_mul_f32_e32 v2, 0x4f7ffffe, v2
	v_cvt_u32_f32_e32 v2, v2
	v_mul_lo_u32 v5, v5, v2
	v_mul_hi_u32 v5, v2, v5
	v_add_u32_e32 v2, v2, v5
	s_waitcnt vmcnt(0)
	v_mul_hi_u32 v2, v4, v2
	v_mul_lo_u32 v5, v2, v3
	v_sub_u32_e32 v5, v4, v5
	v_add_u32_e32 v6, 1, v2
	v_cmp_ge_u32_e32 vcc, v5, v3
	v_add_u32_e32 v4, 1, v4
	s_nop 0
	v_cndmask_b32_e32 v2, v2, v6, vcc
	v_sub_u32_e32 v6, v5, v3
	v_cndmask_b32_e32 v5, v5, v6, vcc
	v_add_u32_e32 v6, 1, v2
	v_cmp_ge_u32_e32 vcc, v5, v3
	s_nop 1
	v_cndmask_b32_e32 v2, v2, v6, vcc
	v_mul_lo_u32 v5, v3, v2
	v_add_u32_e32 v3, v5, v3
	v_cmp_ne_u32_e32 vcc, v4, v3
	s_and_saveexec_b64 s[4:5], vcc
	s_xor_b64 s[4:5], exec, s[4:5]
	s_cbranch_execz .LBB0_3045
	s_waitcnt lgkmcnt(0)
	v_mov_b32_e32 v1, 0x2000
	global_load_dword v1, v1, s[2:3] offset:1024 sc1
	s_add_u32 s12, s2, 0x2400
	s_addc_u32 s13, s3, 0
	s_waitcnt vmcnt(0)
	v_cmp_eq_u32_e32 vcc, v1, v2
	s_and_saveexec_b64 s[6:7], vcc
	s_cbranch_execz .LBB0_3044
	s_add_u32 s10, s94, 0x4200
	s_addc_u32 s11, s95, 0
	s_mov_b32 s24, 1
	s_mov_b64 s[14:15], 0
	v_mov_b32_e32 v1, 0
	s_branch .LBB0_3035

.LBB0_3601:
	v_readlane_b32 s0, v254, 37
	s_lshl_b32 s0, s0, 8
	v_readlane_b32 s4, v254, 34
	v_readlane_b32 s5, v254, 35
	s_add_u32 s0, s4, s0
	s_addc_u32 s1, s5, 0
	buffer_inv sc1
	v_mov_b32_e32 v2, 0x1000
	v_mov_b32_e32 v4, 1
	global_atomic_add v4, v2, v4, s[0:1] offset:1024 sc0
	v_cvt_f32_u32_e32 v2, v3
	v_sub_u32_e32 v5, 0, v3
	v_rcp_iflag_f32_e32 v2, v2
	s_nop 0
	v_mul_f32_e32 v2, 0x4f7ffffe, v2
	v_cvt_u32_f32_e32 v2, v2
	v_mul_lo_u32 v5, v5, v2
	v_mul_hi_u32 v5, v2, v5
	v_add_u32_e32 v2, v2, v5
	s_waitcnt vmcnt(0)
	v_mul_hi_u32 v2, v4, v2
	v_mul_lo_u32 v5, v2, v3
	v_sub_u32_e32 v5, v4, v5
	v_add_u32_e32 v6, 1, v2
	v_cmp_ge_u32_e32 vcc, v5, v3
	v_add_u32_e32 v4, 1, v4
	s_nop 0
	v_cndmask_b32_e32 v2, v2, v6, vcc
	v_sub_u32_e32 v6, v5, v3
	v_cndmask_b32_e32 v5, v5, v6, vcc
	v_add_u32_e32 v6, 1, v2
	v_cmp_ge_u32_e32 vcc, v5, v3
	s_nop 1
	v_cndmask_b32_e32 v2, v2, v6, vcc
	v_mul_lo_u32 v5, v3, v2
	v_add_u32_e32 v3, v5, v3
	v_cmp_ne_u32_e32 vcc, v4, v3
	s_and_saveexec_b64 s[4:5], vcc
	s_xor_b64 s[4:5], exec, s[4:5]
	s_cbranch_execz .LBB0_3615
	s_waitcnt lgkmcnt(0)
	v_mov_b32_e32 v1, 0x2000
	global_load_dword v1, v1, s[0:1] offset:1024 sc1
	s_add_u32 s12, s0, 0x2400
	s_addc_u32 s13, s1, 0
	s_waitcnt vmcnt(0)
	v_cmp_eq_u32_e32 vcc, v1, v2
	s_and_saveexec_b64 s[6:7], vcc
	s_cbranch_execz .LBB0_3614
	s_add_u32 s10, s94, 0x4200
	s_addc_u32 s11, s95, 0
	s_mov_b32 s24, 1
	s_mov_b64 s[14:15], 0
	v_mov_b32_e32 v1, 0
	s_branch .LBB0_3605
